# v48 + G3 (layer-0 SwiGLU up) epilogue rewritten by hand: rstd8 quad sums by DPP instead of chained LDS shuffles, a*b products under the SS load latency, same trimmed f32 silu algebra and pipelined bpe
# speedup vs baseline: 1.0166x; 1.0031x over previous
; __device__ __forceinline__ void rstd8(const float* SS, int rowb, int lane, float (&rs)[2][4]) {
;     f32x4 p[2][4];
; #pragma unroll
;     for (int ai = 0; ai < 2; ++ai)
; #pragma unroll
;         for (int m = 0; m < 4; ++m) p[ai][m] = *(const f32x4*)(SS + (size_t)(rowb + HALF * ai + 16 * m + (lane >> 2)) * 16 + 4 * (lane & 3));
;     asm volatile("" : "+v"(p[0][0]), "+v"(p[0][1]), "+v"(p[0][2]), "+v"(p[0][3]), "+v"(p[1][0]), "+v"(p[1][1]), "+v"(p[1][2]), "+v"(p[1][3]));
; #pragma unroll
;     for (int ai = 0; ai < 2; ++ai)
; #pragma unroll
;         for (int m = 0; m < 4; ++m) { float s = (p[ai][m][0] + p[ai][m][1]) + (p[ai][m][2] + p[ai][m][3]); s += __shfl_xor(s, 1); s += __shfl_xor(s, 2);
;             const float r = __builtin_amdgcn_rsqf(s * (1.0f / 1024.0f) + RMS_EPS);
;             rs[ai][m] = __builtin_bit_cast(float, __builtin_amdgcn_ds_bpermute((lane & 15) << 4, __builtin_bit_cast(int, r))); }
;     __device__ __forceinline__ void operator()(const f32x4 (&acc)[2][2][4][2], const Unit& u, int wr, int wc, int fr, int fq) const {
;     ...
;             for (int m = 0; m < 4; ++m) { const int row = row0 + ai * HALF + m * 16; const float rs = rs8[ai][m];
;                 const f32x4 a0 = acc[ai][0][m][0] * rs, a1 = acc[ai][0][m][1] * rs, b0 = acc[ai][1][m][0] * rs, b1 = acc[ai][1][m][1] * rs;
.LBB0_724:
	v_lshl_add_u32 v182, s20, 8, v175
	v_ashrrev_i32_e32 v183, 31, v182
	v_lshlrev_b64 v[130:131], 6, v[182:183]
	v_lshl_add_u64 v[130:131], v[150:151], 0, v[130:131]
	v_add_co_u32_e32 v132, vcc, 0x2000, v130
	v_addc_co_u32_e32 v133, vcc, 0, v131, vcc
	global_load_dwordx4 v[192:195], v[130:131], off
	global_load_dwordx4 v[196:199], v[130:131], off offset:1024
	global_load_dwordx4 v[200:203], v[130:131], off offset:2048
	global_load_dwordx4 v[204:207], v[130:131], off offset:3072
	global_load_dwordx4 v[208:211], v[132:133], off
	global_load_dwordx4 v[212:215], v[132:133], off offset:1024
	global_load_dwordx4 v[216:219], v[132:133], off offset:2048
	global_load_dwordx4 v[220:223], v[132:133], off offset:3072
	v_lshl_or_b32 v184, s21, 7, v181
	v_ashrrev_i32_e32 v185, 31, v184
	v_mov_b64_e32 v[134:135], s[44:45]
	v_lshlrev_b64 v[184:185], 1, v[184:185]
	v_mad_i64_i32 v[224:225], s[20:21], v182, s49, v[134:135]
	s_nop 0
	v_lshl_add_u64 v[224:225], v[224:225], 0, v[184:185]
	v_pk_mul_f32 v[118:119], v[118:119], v[126:127]
	v_pk_mul_f32 v[120:121], v[120:121], v[128:129]
	v_pk_mul_f32 v[114:115], v[114:115], v[122:123]
	v_pk_mul_f32 v[116:117], v[116:117], v[124:125]
	v_pk_mul_f32 v[102:103], v[102:103], v[110:111]
	v_pk_mul_f32 v[104:105], v[104:105], v[112:113]
	v_pk_mul_f32 v[98:99], v[98:99], v[106:107]
	v_pk_mul_f32 v[100:101], v[100:101], v[108:109]
	v_pk_mul_f32 v[86:87], v[86:87], v[94:95]
	v_pk_mul_f32 v[88:89], v[88:89], v[96:97]
	v_pk_mul_f32 v[82:83], v[82:83], v[90:91]
	v_pk_mul_f32 v[84:85], v[84:85], v[92:93]
	v_pk_mul_f32 v[70:71], v[70:71], v[78:79]
	v_pk_mul_f32 v[72:73], v[72:73], v[80:81]
	v_pk_mul_f32 v[66:67], v[66:67], v[74:75]
	v_pk_mul_f32 v[68:69], v[68:69], v[76:77]
	v_pk_mul_f32 v[54:55], v[54:55], v[62:63]
	v_pk_mul_f32 v[56:57], v[56:57], v[64:65]
	v_pk_mul_f32 v[50:51], v[50:51], v[58:59]
	v_pk_mul_f32 v[52:53], v[52:53], v[60:61]
	v_pk_mul_f32 v[38:39], v[38:39], v[46:47]
	v_pk_mul_f32 v[40:41], v[40:41], v[48:49]
	v_pk_mul_f32 v[34:35], v[34:35], v[42:43]
	v_pk_mul_f32 v[36:37], v[36:37], v[44:45]
	v_pk_mul_f32 v[22:23], v[22:23], v[30:31]
	v_pk_mul_f32 v[24:25], v[24:25], v[32:33]
	v_pk_mul_f32 v[18:19], v[18:19], v[26:27]
	v_pk_mul_f32 v[20:21], v[20:21], v[28:29]
	v_pk_mul_f32 v[6:7], v[6:7], v[14:15]
	v_pk_mul_f32 v[8:9], v[8:9], v[16:17]
	v_pk_mul_f32 v[2:3], v[2:3], v[10:11]
	v_pk_mul_f32 v[4:5], v[4:5], v[12:13]
	s_waitcnt vmcnt(0)
	v_add_f32_e32 v192, v192, v193
	v_add_f32_e32 v196, v196, v197
	v_add_f32_e32 v200, v200, v201
	v_add_f32_e32 v204, v204, v205
	v_add_f32_e32 v208, v208, v209
	v_add_f32_e32 v212, v212, v213
	v_add_f32_e32 v216, v216, v217
	v_add_f32_e32 v220, v220, v221
	v_add_f32_e32 v194, v194, v195
	v_add_f32_e32 v198, v198, v199
	v_add_f32_e32 v202, v202, v203
	v_add_f32_e32 v206, v206, v207
	v_add_f32_e32 v210, v210, v211
	v_add_f32_e32 v214, v214, v215
	v_add_f32_e32 v218, v218, v219
	v_add_f32_e32 v222, v222, v223
	v_add_f32_e32 v192, v192, v194
	v_add_f32_e32 v196, v196, v198
	v_add_f32_e32 v200, v200, v202
	v_add_f32_e32 v204, v204, v206
	v_add_f32_e32 v208, v208, v210
	v_add_f32_e32 v212, v212, v214
	v_add_f32_e32 v216, v216, v218
	v_add_f32_e32 v220, v220, v222
	v_add_f32_dpp v192, v192, v192 quad_perm:[1,0,3,2] row_mask:0xf bank_mask:0xf
	v_add_f32_dpp v196, v196, v196 quad_perm:[1,0,3,2] row_mask:0xf bank_mask:0xf
	v_add_f32_dpp v200, v200, v200 quad_perm:[1,0,3,2] row_mask:0xf bank_mask:0xf
	v_add_f32_dpp v204, v204, v204 quad_perm:[1,0,3,2] row_mask:0xf bank_mask:0xf
	v_add_f32_dpp v208, v208, v208 quad_perm:[1,0,3,2] row_mask:0xf bank_mask:0xf
	v_add_f32_dpp v212, v212, v212 quad_perm:[1,0,3,2] row_mask:0xf bank_mask:0xf
	v_add_f32_dpp v216, v216, v216 quad_perm:[1,0,3,2] row_mask:0xf bank_mask:0xf
	v_add_f32_dpp v220, v220, v220 quad_perm:[1,0,3,2] row_mask:0xf bank_mask:0xf
	v_add_f32_dpp v192, v192, v192 quad_perm:[2,3,0,1] row_mask:0xf bank_mask:0xf
	v_add_f32_dpp v196, v196, v196 quad_perm:[2,3,0,1] row_mask:0xf bank_mask:0xf
	v_add_f32_dpp v200, v200, v200 quad_perm:[2,3,0,1] row_mask:0xf bank_mask:0xf
	v_add_f32_dpp v204, v204, v204 quad_perm:[2,3,0,1] row_mask:0xf bank_mask:0xf
	v_add_f32_dpp v208, v208, v208 quad_perm:[2,3,0,1] row_mask:0xf bank_mask:0xf
	v_add_f32_dpp v212, v212, v212 quad_perm:[2,3,0,1] row_mask:0xf bank_mask:0xf
	v_add_f32_dpp v216, v216, v216 quad_perm:[2,3,0,1] row_mask:0xf bank_mask:0xf
	v_add_f32_dpp v220, v220, v220 quad_perm:[2,3,0,1] row_mask:0xf bank_mask:0xf
	v_fmamk_f32 v192, v192, 0x3a800000, v190
	v_fmamk_f32 v196, v196, 0x3a800000, v190
	v_fmamk_f32 v200, v200, 0x3a800000, v190
	v_fmamk_f32 v204, v204, 0x3a800000, v190
	v_fmamk_f32 v208, v208, 0x3a800000, v190
	v_fmamk_f32 v212, v212, 0x3a800000, v190
	v_fmamk_f32 v216, v216, 0x3a800000, v190
	v_fmamk_f32 v220, v220, 0x3a800000, v190
	ds_bpermute_b32 v192, v179, v192
	ds_bpermute_b32 v196, v179, v196
	ds_bpermute_b32 v200, v179, v200
	ds_bpermute_b32 v204, v179, v204
	ds_bpermute_b32 v208, v179, v208
	ds_bpermute_b32 v212, v179, v212
	ds_bpermute_b32 v216, v179, v216
	ds_bpermute_b32 v220, v179, v220
	s_waitcnt lgkmcnt(0)
; __device__ __forceinline__ unsigned cvt_pk_bf16(float lo, float hi) { const f32x2c_t v = {lo, hi}; return __builtin_bit_cast(unsigned, __builtin_convertvector(v, bf16x2c_t)); }
; __device__ __forceinline__ float silu_f(float a) { return a * __builtin_amdgcn_rcpf(1.0f + __builtin_amdgcn_exp2f(a * -1.4426950408889634f)); }
;     __device__ __forceinline__ void operator()(const f32x4 (&acc)[2][2][4][2], const Unit& u, int wr, int wc, int fr, int fq) const {
;     ...
;         for (int ai = 0; ai < 2; ++ai) {
; #pragma unroll
;             for (int m = 0; m < 4; ++m) { const int row = row0 + ai * HALF + m * 16; const float rs = rs8[ai][m];
;                 const f32x4 a0 = acc[ai][0][m][0] * rs, a1 = acc[ai][0][m][1] * rs, b0 = acc[ai][1][m][0] * rs, b1 = acc[ai][1][m][1] * rs;
;                 f32x4 g0, g1;
; #pragma unroll
;                 for (int j = 0; j < 4; ++j) { g0[j] = silu_f(a0[j]) * b0[j]; g1[j] = silu_f(a1[j]) * b1[j]; }
;                 u32x4 w; w.x = cvt_pk_bf16(g0[0], g0[1]); w.y = cvt_pk_bf16(g0[2], g0[3]); w.z = cvt_pk_bf16(g1[0], g1[1]); w.w = cvt_pk_bf16(g1[2], g1[3]);
;                 w = lane_perm(w, qs4); u32x4* dst = (u32x4*)(O + (size_t)(rowS + ai * HALF + m * 16) * ldo + colS); (void)row;
;                 if constexpr (MOE) __builtin_nontemporal_store(w, dst); else *dst = w; } }
	v_rsq_f32_e32 v194, v192
	v_rsq_f32_e32 v198, v196
	v_rsq_f32_e32 v202, v200
	v_rsq_f32_e32 v206, v204
	v_rsq_f32_e32 v210, v208
	v_rsq_f32_e32 v214, v212
	v_rsq_f32_e32 v218, v216
	v_rsq_f32_e32 v222, v220
	v_mul_f32_e32 v194, 0xbfb8aa3b, v194
	v_mul_f32_e32 v198, 0xbfb8aa3b, v198
	v_mul_f32_e32 v202, 0xbfb8aa3b, v202
	v_mul_f32_e32 v206, 0xbfb8aa3b, v206
	v_mul_f32_e32 v210, 0xbfb8aa3b, v210
	v_mul_f32_e32 v214, 0xbfb8aa3b, v214
	v_mul_f32_e32 v218, 0xbfb8aa3b, v218
	v_mul_f32_e32 v222, 0xbfb8aa3b, v222
	v_pk_mul_f32 v[126:127], v[126:127], v[194:195] op_sel_hi:[1,0]
	v_pk_mul_f32 v[128:129], v[128:129], v[194:195] op_sel_hi:[1,0]
	v_pk_mul_f32 v[122:123], v[122:123], v[194:195] op_sel_hi:[1,0]
	v_pk_mul_f32 v[124:125], v[124:125], v[194:195] op_sel_hi:[1,0]
	v_exp_f32_e32 v126, v126
	v_exp_f32_e32 v127, v127
	v_exp_f32_e32 v128, v128
	v_exp_f32_e32 v129, v129
	v_exp_f32_e32 v122, v122
	v_exp_f32_e32 v123, v123
	v_exp_f32_e32 v124, v124
	v_exp_f32_e32 v125, v125
	v_pk_fma_f32 v[126:127], v[126:127], v[192:193], v[192:193] op_sel_hi:[1,0,0]
	v_pk_fma_f32 v[128:129], v[128:129], v[192:193], v[192:193] op_sel_hi:[1,0,0]
	v_pk_fma_f32 v[122:123], v[122:123], v[192:193], v[192:193] op_sel_hi:[1,0,0]
	v_pk_fma_f32 v[124:125], v[124:125], v[192:193], v[192:193] op_sel_hi:[1,0,0]
	v_rcp_f32_e32 v126, v126
	v_rcp_f32_e32 v127, v127
	v_rcp_f32_e32 v128, v128
	v_rcp_f32_e32 v129, v129
	v_rcp_f32_e32 v122, v122
	v_rcp_f32_e32 v123, v123
	v_rcp_f32_e32 v124, v124
	v_rcp_f32_e32 v125, v125
	v_pk_mul_f32 v[118:119], v[118:119], v[126:127]
	v_pk_mul_f32 v[120:121], v[120:121], v[128:129]
	v_pk_mul_f32 v[114:115], v[114:115], v[122:123]
	v_pk_mul_f32 v[116:117], v[116:117], v[124:125]
	v_cvt_pk_bf16_f32 v126, v118, v119
	v_cvt_pk_bf16_f32 v127, v120, v121
	v_cvt_pk_bf16_f32 v128, v114, v115
	v_cvt_pk_bf16_f32 v129, v116, v117
	ds_bpermute_b32 v122, v171, v126
	ds_bpermute_b32 v123, v171, v127
	ds_bpermute_b32 v124, v171, v128
	ds_bpermute_b32 v125, v171, v129
	v_mov_b32_e32 v226, v224
	v_mov_b32_e32 v227, v225
	v_pk_mul_f32 v[110:111], v[110:111], v[198:199] op_sel_hi:[1,0]
	v_pk_mul_f32 v[112:113], v[112:113], v[198:199] op_sel_hi:[1,0]
	v_pk_mul_f32 v[106:107], v[106:107], v[198:199] op_sel_hi:[1,0]
	v_pk_mul_f32 v[108:109], v[108:109], v[198:199] op_sel_hi:[1,0]
	v_exp_f32_e32 v110, v110
	v_exp_f32_e32 v111, v111
	v_exp_f32_e32 v112, v112
	v_exp_f32_e32 v113, v113
	v_exp_f32_e32 v106, v106
	v_exp_f32_e32 v107, v107
	v_exp_f32_e32 v108, v108
	v_exp_f32_e32 v109, v109
	v_pk_fma_f32 v[110:111], v[110:111], v[196:197], v[196:197] op_sel_hi:[1,0,0]
	v_pk_fma_f32 v[112:113], v[112:113], v[196:197], v[196:197] op_sel_hi:[1,0,0]
	v_pk_fma_f32 v[106:107], v[106:107], v[196:197], v[196:197] op_sel_hi:[1,0,0]
	v_pk_fma_f32 v[108:109], v[108:109], v[196:197], v[196:197] op_sel_hi:[1,0,0]
	v_rcp_f32_e32 v110, v110
	v_rcp_f32_e32 v111, v111
	v_rcp_f32_e32 v112, v112
	v_rcp_f32_e32 v113, v113
	v_rcp_f32_e32 v106, v106
	v_rcp_f32_e32 v107, v107
	v_rcp_f32_e32 v108, v108
	v_rcp_f32_e32 v109, v109
	v_pk_mul_f32 v[102:103], v[102:103], v[110:111]
	v_pk_mul_f32 v[104:105], v[104:105], v[112:113]
	v_pk_mul_f32 v[98:99], v[98:99], v[106:107]
	v_pk_mul_f32 v[100:101], v[100:101], v[108:109]
	s_waitcnt lgkmcnt(0)
	global_store_dwordx4 v[226:227], v[122:125], off
	v_cvt_pk_bf16_f32 v110, v102, v103
	v_cvt_pk_bf16_f32 v111, v104, v105
	v_cvt_pk_bf16_f32 v112, v98, v99
	v_cvt_pk_bf16_f32 v113, v100, v101
	ds_bpermute_b32 v106, v171, v110
	ds_bpermute_b32 v107, v171, v111
	ds_bpermute_b32 v108, v171, v112
	ds_bpermute_b32 v109, v171, v113
	v_add_co_u32_e32 v230, vcc, 0x16000, v224
	v_addc_co_u32_e32 v231, vcc, 0, v225, vcc
	v_pk_mul_f32 v[94:95], v[94:95], v[202:203] op_sel_hi:[1,0]
	v_pk_mul_f32 v[96:97], v[96:97], v[202:203] op_sel_hi:[1,0]
	v_pk_mul_f32 v[90:91], v[90:91], v[202:203] op_sel_hi:[1,0]
	v_pk_mul_f32 v[92:93], v[92:93], v[202:203] op_sel_hi:[1,0]
	v_exp_f32_e32 v94, v94
	v_exp_f32_e32 v95, v95
	v_exp_f32_e32 v96, v96
	v_exp_f32_e32 v97, v97
	v_exp_f32_e32 v90, v90
	v_exp_f32_e32 v91, v91
	v_exp_f32_e32 v92, v92
	v_exp_f32_e32 v93, v93
	v_pk_fma_f32 v[94:95], v[94:95], v[200:201], v[200:201] op_sel_hi:[1,0,0]
	v_pk_fma_f32 v[96:97], v[96:97], v[200:201], v[200:201] op_sel_hi:[1,0,0]
	v_pk_fma_f32 v[90:91], v[90:91], v[200:201], v[200:201] op_sel_hi:[1,0,0]
	v_pk_fma_f32 v[92:93], v[92:93], v[200:201], v[200:201] op_sel_hi:[1,0,0]
	v_rcp_f32_e32 v94, v94
	v_rcp_f32_e32 v95, v95
	v_rcp_f32_e32 v96, v96
	v_rcp_f32_e32 v97, v97
	v_rcp_f32_e32 v90, v90
	v_rcp_f32_e32 v91, v91
	v_rcp_f32_e32 v92, v92
	v_rcp_f32_e32 v93, v93
	v_pk_mul_f32 v[86:87], v[86:87], v[94:95]
	v_pk_mul_f32 v[88:89], v[88:89], v[96:97]
	v_pk_mul_f32 v[82:83], v[82:83], v[90:91]
	v_pk_mul_f32 v[84:85], v[84:85], v[92:93]
	s_waitcnt lgkmcnt(0)
	global_store_dwordx4 v[230:231], v[106:109], off
	v_cvt_pk_bf16_f32 v94, v86, v87
	v_cvt_pk_bf16_f32 v95, v88, v89
	v_cvt_pk_bf16_f32 v96, v82, v83
	v_cvt_pk_bf16_f32 v97, v84, v85
	ds_bpermute_b32 v90, v171, v94
	ds_bpermute_b32 v91, v171, v95
	ds_bpermute_b32 v92, v171, v96
	ds_bpermute_b32 v93, v171, v97
	v_add_co_u32_e32 v226, vcc, 0x2c000, v224
	v_addc_co_u32_e32 v227, vcc, 0, v225, vcc
	v_pk_mul_f32 v[78:79], v[78:79], v[206:207] op_sel_hi:[1,0]
	v_pk_mul_f32 v[80:81], v[80:81], v[206:207] op_sel_hi:[1,0]
	v_pk_mul_f32 v[74:75], v[74:75], v[206:207] op_sel_hi:[1,0]
	v_pk_mul_f32 v[76:77], v[76:77], v[206:207] op_sel_hi:[1,0]
	v_exp_f32_e32 v78, v78
	v_exp_f32_e32 v79, v79
	v_exp_f32_e32 v80, v80
	v_exp_f32_e32 v81, v81
	v_exp_f32_e32 v74, v74
	v_exp_f32_e32 v75, v75
	v_exp_f32_e32 v76, v76
	v_exp_f32_e32 v77, v77
	v_pk_fma_f32 v[78:79], v[78:79], v[204:205], v[204:205] op_sel_hi:[1,0,0]
	v_pk_fma_f32 v[80:81], v[80:81], v[204:205], v[204:205] op_sel_hi:[1,0,0]
	v_pk_fma_f32 v[74:75], v[74:75], v[204:205], v[204:205] op_sel_hi:[1,0,0]
	v_pk_fma_f32 v[76:77], v[76:77], v[204:205], v[204:205] op_sel_hi:[1,0,0]
	v_rcp_f32_e32 v78, v78
	v_rcp_f32_e32 v79, v79
	v_rcp_f32_e32 v80, v80
	v_rcp_f32_e32 v81, v81
	v_rcp_f32_e32 v74, v74
	v_rcp_f32_e32 v75, v75
	v_rcp_f32_e32 v76, v76
	v_rcp_f32_e32 v77, v77
	v_pk_mul_f32 v[70:71], v[70:71], v[78:79]
	v_pk_mul_f32 v[72:73], v[72:73], v[80:81]
	v_pk_mul_f32 v[66:67], v[66:67], v[74:75]
	v_pk_mul_f32 v[68:69], v[68:69], v[76:77]
	s_waitcnt lgkmcnt(0)
; __device__ __forceinline__ unsigned cvt_pk_bf16(float lo, float hi) { const f32x2c_t v = {lo, hi}; return __builtin_bit_cast(unsigned, __builtin_convertvector(v, bf16x2c_t)); }
; __device__ __forceinline__ float silu_f(float a) { return a * __builtin_amdgcn_rcpf(1.0f + __builtin_amdgcn_exp2f(a * -1.4426950408889634f)); }
;     __device__ __forceinline__ void operator()(const f32x4 (&acc)[2][2][4][2], const Unit& u, int wr, int wc, int fr, int fq) const {
;     ...
;         for (int ai = 0; ai < 2; ++ai) {
; #pragma unroll
;             for (int m = 0; m < 4; ++m) { const int row = row0 + ai * HALF + m * 16; const float rs = rs8[ai][m];
;                 const f32x4 a0 = acc[ai][0][m][0] * rs, a1 = acc[ai][0][m][1] * rs, b0 = acc[ai][1][m][0] * rs, b1 = acc[ai][1][m][1] * rs;
;                 f32x4 g0, g1;
; #pragma unroll
;                 for (int j = 0; j < 4; ++j) { g0[j] = silu_f(a0[j]) * b0[j]; g1[j] = silu_f(a1[j]) * b1[j]; }
;                 u32x4 w; w.x = cvt_pk_bf16(g0[0], g0[1]); w.y = cvt_pk_bf16(g0[2], g0[3]); w.z = cvt_pk_bf16(g1[0], g1[1]); w.w = cvt_pk_bf16(g1[2], g1[3]);
;                 w = lane_perm(w, qs4); u32x4* dst = (u32x4*)(O + (size_t)(rowS + ai * HALF + m * 16) * ldo + colS); (void)row;
;                 if constexpr (MOE) __builtin_nontemporal_store(w, dst); else *dst = w; } }
	global_store_dwordx4 v[226:227], v[90:93], off
	v_cvt_pk_bf16_f32 v78, v70, v71
	v_cvt_pk_bf16_f32 v79, v72, v73
	v_cvt_pk_bf16_f32 v80, v66, v67
	v_cvt_pk_bf16_f32 v81, v68, v69
	ds_bpermute_b32 v74, v171, v78
	ds_bpermute_b32 v75, v171, v79
	ds_bpermute_b32 v76, v171, v80
	ds_bpermute_b32 v77, v171, v81
	v_add_co_u32_e32 v230, vcc, 0x42000, v224
	v_addc_co_u32_e32 v231, vcc, 0, v225, vcc
	v_pk_mul_f32 v[62:63], v[62:63], v[210:211] op_sel_hi:[1,0]
	v_pk_mul_f32 v[64:65], v[64:65], v[210:211] op_sel_hi:[1,0]
	v_pk_mul_f32 v[58:59], v[58:59], v[210:211] op_sel_hi:[1,0]
	v_pk_mul_f32 v[60:61], v[60:61], v[210:211] op_sel_hi:[1,0]
	v_exp_f32_e32 v62, v62
	v_exp_f32_e32 v63, v63
	v_exp_f32_e32 v64, v64
	v_exp_f32_e32 v65, v65
	v_exp_f32_e32 v58, v58
	v_exp_f32_e32 v59, v59
	v_exp_f32_e32 v60, v60
	v_exp_f32_e32 v61, v61
	v_pk_fma_f32 v[62:63], v[62:63], v[208:209], v[208:209] op_sel_hi:[1,0,0]
	v_pk_fma_f32 v[64:65], v[64:65], v[208:209], v[208:209] op_sel_hi:[1,0,0]
	v_pk_fma_f32 v[58:59], v[58:59], v[208:209], v[208:209] op_sel_hi:[1,0,0]
	v_pk_fma_f32 v[60:61], v[60:61], v[208:209], v[208:209] op_sel_hi:[1,0,0]
	v_rcp_f32_e32 v62, v62
	v_rcp_f32_e32 v63, v63
	v_rcp_f32_e32 v64, v64
	v_rcp_f32_e32 v65, v65
	v_rcp_f32_e32 v58, v58
	v_rcp_f32_e32 v59, v59
	v_rcp_f32_e32 v60, v60
	v_rcp_f32_e32 v61, v61
	v_pk_mul_f32 v[54:55], v[54:55], v[62:63]
	v_pk_mul_f32 v[56:57], v[56:57], v[64:65]
	v_pk_mul_f32 v[50:51], v[50:51], v[58:59]
	v_pk_mul_f32 v[52:53], v[52:53], v[60:61]
	s_waitcnt lgkmcnt(0)
	global_store_dwordx4 v[230:231], v[74:77], off
	v_cvt_pk_bf16_f32 v62, v54, v55
	v_cvt_pk_bf16_f32 v63, v56, v57
	v_cvt_pk_bf16_f32 v64, v50, v51
	v_cvt_pk_bf16_f32 v65, v52, v53
	ds_bpermute_b32 v58, v171, v62
	ds_bpermute_b32 v59, v171, v63
	ds_bpermute_b32 v60, v171, v64
	ds_bpermute_b32 v61, v171, v65
	v_add_co_u32_e32 v226, vcc, 0xb0000, v224
	v_addc_co_u32_e32 v227, vcc, 0, v225, vcc
	v_pk_mul_f32 v[46:47], v[46:47], v[214:215] op_sel_hi:[1,0]
	v_pk_mul_f32 v[48:49], v[48:49], v[214:215] op_sel_hi:[1,0]
	v_pk_mul_f32 v[42:43], v[42:43], v[214:215] op_sel_hi:[1,0]
	v_pk_mul_f32 v[44:45], v[44:45], v[214:215] op_sel_hi:[1,0]
	v_exp_f32_e32 v46, v46
	v_exp_f32_e32 v47, v47
	v_exp_f32_e32 v48, v48
	v_exp_f32_e32 v49, v49
	v_exp_f32_e32 v42, v42
	v_exp_f32_e32 v43, v43
	v_exp_f32_e32 v44, v44
	v_exp_f32_e32 v45, v45
	v_pk_fma_f32 v[46:47], v[46:47], v[212:213], v[212:213] op_sel_hi:[1,0,0]
	v_pk_fma_f32 v[48:49], v[48:49], v[212:213], v[212:213] op_sel_hi:[1,0,0]
	v_pk_fma_f32 v[42:43], v[42:43], v[212:213], v[212:213] op_sel_hi:[1,0,0]
	v_pk_fma_f32 v[44:45], v[44:45], v[212:213], v[212:213] op_sel_hi:[1,0,0]
	v_rcp_f32_e32 v46, v46
	v_rcp_f32_e32 v47, v47
	v_rcp_f32_e32 v48, v48
	v_rcp_f32_e32 v49, v49
	v_rcp_f32_e32 v42, v42
	v_rcp_f32_e32 v43, v43
	v_rcp_f32_e32 v44, v44
	v_rcp_f32_e32 v45, v45
	v_pk_mul_f32 v[38:39], v[38:39], v[46:47]
	v_pk_mul_f32 v[40:41], v[40:41], v[48:49]
	v_pk_mul_f32 v[34:35], v[34:35], v[42:43]
	v_pk_mul_f32 v[36:37], v[36:37], v[44:45]
	s_waitcnt lgkmcnt(0)
	global_store_dwordx4 v[226:227], v[58:61], off
	v_cvt_pk_bf16_f32 v46, v38, v39
	v_cvt_pk_bf16_f32 v47, v40, v41
	v_cvt_pk_bf16_f32 v48, v34, v35
	v_cvt_pk_bf16_f32 v49, v36, v37
	ds_bpermute_b32 v42, v171, v46
	ds_bpermute_b32 v43, v171, v47
	ds_bpermute_b32 v44, v171, v48
	ds_bpermute_b32 v45, v171, v49
	v_add_co_u32_e32 v230, vcc, 0xc6000, v224
	v_addc_co_u32_e32 v231, vcc, 0, v225, vcc
	v_pk_mul_f32 v[30:31], v[30:31], v[218:219] op_sel_hi:[1,0]
	v_pk_mul_f32 v[32:33], v[32:33], v[218:219] op_sel_hi:[1,0]
	v_pk_mul_f32 v[26:27], v[26:27], v[218:219] op_sel_hi:[1,0]
	v_pk_mul_f32 v[28:29], v[28:29], v[218:219] op_sel_hi:[1,0]
	v_exp_f32_e32 v30, v30
	v_exp_f32_e32 v31, v31
	v_exp_f32_e32 v32, v32
	v_exp_f32_e32 v33, v33
	v_exp_f32_e32 v26, v26
	v_exp_f32_e32 v27, v27
	v_exp_f32_e32 v28, v28
	v_exp_f32_e32 v29, v29
	v_pk_fma_f32 v[30:31], v[30:31], v[216:217], v[216:217] op_sel_hi:[1,0,0]
	v_pk_fma_f32 v[32:33], v[32:33], v[216:217], v[216:217] op_sel_hi:[1,0,0]
	v_pk_fma_f32 v[26:27], v[26:27], v[216:217], v[216:217] op_sel_hi:[1,0,0]
	v_pk_fma_f32 v[28:29], v[28:29], v[216:217], v[216:217] op_sel_hi:[1,0,0]
	v_rcp_f32_e32 v30, v30
	v_rcp_f32_e32 v31, v31
	v_rcp_f32_e32 v32, v32
	v_rcp_f32_e32 v33, v33
	v_rcp_f32_e32 v26, v26
	v_rcp_f32_e32 v27, v27
	v_rcp_f32_e32 v28, v28
	v_rcp_f32_e32 v29, v29
	v_pk_mul_f32 v[22:23], v[22:23], v[30:31]
	v_pk_mul_f32 v[24:25], v[24:25], v[32:33]
	v_pk_mul_f32 v[18:19], v[18:19], v[26:27]
	v_pk_mul_f32 v[20:21], v[20:21], v[28:29]
	s_waitcnt lgkmcnt(0)
	global_store_dwordx4 v[230:231], v[42:45], off
	v_cvt_pk_bf16_f32 v30, v22, v23
	v_cvt_pk_bf16_f32 v31, v24, v25
	v_cvt_pk_bf16_f32 v32, v18, v19
	v_cvt_pk_bf16_f32 v33, v20, v21
	ds_bpermute_b32 v26, v171, v30
	ds_bpermute_b32 v27, v171, v31
	ds_bpermute_b32 v28, v171, v32
	ds_bpermute_b32 v29, v171, v33
	v_add_co_u32_e32 v226, vcc, 0xdc000, v224
	v_addc_co_u32_e32 v227, vcc, 0, v225, vcc
	v_pk_mul_f32 v[14:15], v[14:15], v[222:223] op_sel_hi:[1,0]
	v_pk_mul_f32 v[16:17], v[16:17], v[222:223] op_sel_hi:[1,0]
	v_pk_mul_f32 v[10:11], v[10:11], v[222:223] op_sel_hi:[1,0]
	v_pk_mul_f32 v[12:13], v[12:13], v[222:223] op_sel_hi:[1,0]
	v_exp_f32_e32 v14, v14
	v_exp_f32_e32 v15, v15
	v_exp_f32_e32 v16, v16
	v_exp_f32_e32 v17, v17
	v_exp_f32_e32 v10, v10
	v_exp_f32_e32 v11, v11
	v_exp_f32_e32 v12, v12
	v_exp_f32_e32 v13, v13
	v_pk_fma_f32 v[14:15], v[14:15], v[220:221], v[220:221] op_sel_hi:[1,0,0]
	v_pk_fma_f32 v[16:17], v[16:17], v[220:221], v[220:221] op_sel_hi:[1,0,0]
	v_pk_fma_f32 v[10:11], v[10:11], v[220:221], v[220:221] op_sel_hi:[1,0,0]
	v_pk_fma_f32 v[12:13], v[12:13], v[220:221], v[220:221] op_sel_hi:[1,0,0]
	v_rcp_f32_e32 v14, v14
	v_rcp_f32_e32 v15, v15
	v_rcp_f32_e32 v16, v16
	v_rcp_f32_e32 v17, v17
	v_rcp_f32_e32 v10, v10
	v_rcp_f32_e32 v11, v11
	v_rcp_f32_e32 v12, v12
	v_rcp_f32_e32 v13, v13
	v_pk_mul_f32 v[6:7], v[6:7], v[14:15]
	v_pk_mul_f32 v[8:9], v[8:9], v[16:17]
	v_pk_mul_f32 v[2:3], v[2:3], v[10:11]
	v_pk_mul_f32 v[4:5], v[4:5], v[12:13]
	s_waitcnt lgkmcnt(0)
	global_store_dwordx4 v[226:227], v[26:29], off
	v_cvt_pk_bf16_f32 v14, v6, v7
	v_cvt_pk_bf16_f32 v15, v8, v9
	v_cvt_pk_bf16_f32 v16, v2, v3
	v_cvt_pk_bf16_f32 v17, v4, v5
	ds_bpermute_b32 v10, v171, v14
	ds_bpermute_b32 v11, v171, v15
	ds_bpermute_b32 v12, v171, v16
	ds_bpermute_b32 v13, v171, v17
	v_add_co_u32_e32 v230, vcc, 0xf2000, v224
	v_addc_co_u32_e32 v231, vcc, 0, v225, vcc
	s_waitcnt lgkmcnt(0)
	global_store_dwordx4 v[230:231], v[10:13], off
	s_andn2_b64 vcc, exec, s[4:5]
	s_mov_b64 s[20:21], -1
	s_cbranch_vccnz .LBB0_717
	s_andn2_b64 vcc, exec, s[6:7]
	s_cbranch_vccnz .LBB0_716
	s_barrier
	s_branch .LBB0_716
